# baseline (speedup 1.0000x reference)
.Ll2g_prc:
	s_mov_b32 s1, 0
	v_mov_b32_e32 v50, 0
	v_mov_b32_e32 v51, 0
	ds_read2_b64 v[8:11], v6 offset0:0 offset1:1
	ds_read2_b64 v[12:15], v6 offset0:2 offset1:3
	s_waitcnt lgkmcnt(0)
	v_lshl_or_b32 v9, v9, 7, v38
	v_lshl_or_b32 v11, v11, 7, v38
	v_lshl_or_b32 v13, v13, 7, v38
	v_lshl_or_b32 v15, v15, 7, v38
	buffer_load_dwordx2 v[20:21], v9, s[12:15], 0 offen
	buffer_load_dwordx2 v[22:23], v11, s[12:15], 0 offen
	buffer_load_dwordx2 v[24:25], v13, s[12:15], 0 offen
	buffer_load_dwordx2 v[26:27], v15, s[12:15], 0 offen
	v_mov_b32_e32 v40, 0
	v_mov_b32_e32 v41, 0
	v_mov_b32_e32 v42, 0
	v_mov_b32_e32 v43, 0
	v_mov_b32_e32 v44, 0
	v_mov_b32_e32 v45, 0
	v_mov_b32_e32 v46, 0
	v_mov_b32_e32 v47, 0
.Ll2g_loop:
	s_add_i32 s1, s1, 4
	s_cmp_ge_i32 s1, s0
	s_cbranch_scc1 .Ll2g_lastA
	v_cmp_ge_i32_e64 s[24:25], v37, s1
	ds_read2_b64 v[28:31], v6 offset0:4 offset1:5
	ds_read2_b64 v[32:35], v6 offset0:6 offset1:7
	s_waitcnt lgkmcnt(0)
	v_lshl_or_b32 v29, v29, 7, v38
	v_lshl_or_b32 v31, v31, 7, v38
	v_lshl_or_b32 v33, v33, 7, v38
	v_lshl_or_b32 v35, v35, 7, v38
	s_mov_b64 exec, s[24:25]
	buffer_load_dwordx2 v[40:41], v29, s[12:15], 0 offen
	buffer_load_dwordx2 v[42:43], v31, s[12:15], 0 offen
	buffer_load_dwordx2 v[44:45], v33, s[12:15], 0 offen
	buffer_load_dwordx2 v[46:47], v35, s[12:15], 0 offen
	s_mov_b64 exec, -1
	s_waitcnt vmcnt(4)
	v_cvt_f32_f16_sdwa v53, v20 dst_sel:DWORD dst_unused:UNUSED_PAD src0_sel:WORD_1
	v_cvt_f32_f16_e32 v52, v20
	v_cvt_f32_f16_sdwa v55, v21 dst_sel:DWORD dst_unused:UNUSED_PAD src0_sel:WORD_1
	v_cvt_f32_f16_e32 v54, v21
	v_pk_fma_f32 v[48:49], v[8:9], v[52:53], v[48:49] op_sel_hi:[0,1,1]
	v_pk_fma_f32 v[50:51], v[8:9], v[54:55], v[50:51] op_sel_hi:[0,1,1]
	v_cvt_f32_f16_sdwa v57, v22 dst_sel:DWORD dst_unused:UNUSED_PAD src0_sel:WORD_1
	v_cvt_f32_f16_e32 v56, v22
	v_cvt_f32_f16_sdwa v59, v23 dst_sel:DWORD dst_unused:UNUSED_PAD src0_sel:WORD_1
	v_cvt_f32_f16_e32 v58, v23
	v_pk_fma_f32 v[48:49], v[10:11], v[56:57], v[48:49] op_sel_hi:[0,1,1]
	v_pk_fma_f32 v[50:51], v[10:11], v[58:59], v[50:51] op_sel_hi:[0,1,1]
	v_cvt_f32_f16_sdwa v53, v24 dst_sel:DWORD dst_unused:UNUSED_PAD src0_sel:WORD_1
	v_cvt_f32_f16_e32 v52, v24
	v_cvt_f32_f16_sdwa v55, v25 dst_sel:DWORD dst_unused:UNUSED_PAD src0_sel:WORD_1
	v_cvt_f32_f16_e32 v54, v25
	v_pk_fma_f32 v[48:49], v[12:13], v[52:53], v[48:49] op_sel_hi:[0,1,1]
	v_pk_fma_f32 v[50:51], v[12:13], v[54:55], v[50:51] op_sel_hi:[0,1,1]
	v_cvt_f32_f16_sdwa v57, v26 dst_sel:DWORD dst_unused:UNUSED_PAD src0_sel:WORD_1
	v_cvt_f32_f16_e32 v56, v26
	v_cvt_f32_f16_sdwa v59, v27 dst_sel:DWORD dst_unused:UNUSED_PAD src0_sel:WORD_1
	v_cvt_f32_f16_e32 v58, v27
	v_pk_fma_f32 v[48:49], v[14:15], v[56:57], v[48:49] op_sel_hi:[0,1,1]
	v_pk_fma_f32 v[50:51], v[14:15], v[58:59], v[50:51] op_sel_hi:[0,1,1]
	s_add_i32 s1, s1, 4
	s_cmp_ge_i32 s1, s0
	s_cbranch_scc1 .Ll2g_lastB
	v_cmp_ge_i32_e64 s[24:25], v37, s1
	ds_read2_b64 v[8:11], v6 offset0:8 offset1:9
	ds_read2_b64 v[12:15], v6 offset0:10 offset1:11
	v_add_u32_e32 v6, 64, v6
	s_waitcnt lgkmcnt(0)
	v_lshl_or_b32 v9, v9, 7, v38
	v_lshl_or_b32 v11, v11, 7, v38
	v_lshl_or_b32 v13, v13, 7, v38
	v_lshl_or_b32 v15, v15, 7, v38
	s_mov_b64 exec, s[24:25]
	buffer_load_dwordx2 v[20:21], v9, s[12:15], 0 offen
	buffer_load_dwordx2 v[22:23], v11, s[12:15], 0 offen
	buffer_load_dwordx2 v[24:25], v13, s[12:15], 0 offen
	buffer_load_dwordx2 v[26:27], v15, s[12:15], 0 offen
	s_mov_b64 exec, -1
	s_waitcnt vmcnt(4)
	v_cvt_f32_f16_sdwa v53, v40 dst_sel:DWORD dst_unused:UNUSED_PAD src0_sel:WORD_1
	v_cvt_f32_f16_e32 v52, v40
	v_cvt_f32_f16_sdwa v55, v41 dst_sel:DWORD dst_unused:UNUSED_PAD src0_sel:WORD_1
	v_cvt_f32_f16_e32 v54, v41
	v_pk_fma_f32 v[48:49], v[28:29], v[52:53], v[48:49] op_sel_hi:[0,1,1]
	v_pk_fma_f32 v[50:51], v[28:29], v[54:55], v[50:51] op_sel_hi:[0,1,1]
	v_cvt_f32_f16_sdwa v57, v42 dst_sel:DWORD dst_unused:UNUSED_PAD src0_sel:WORD_1
	v_cvt_f32_f16_e32 v56, v42
	v_cvt_f32_f16_sdwa v59, v43 dst_sel:DWORD dst_unused:UNUSED_PAD src0_sel:WORD_1
	v_cvt_f32_f16_e32 v58, v43
	v_pk_fma_f32 v[48:49], v[30:31], v[56:57], v[48:49] op_sel_hi:[0,1,1]
	v_pk_fma_f32 v[50:51], v[30:31], v[58:59], v[50:51] op_sel_hi:[0,1,1]
	v_cvt_f32_f16_sdwa v53, v44 dst_sel:DWORD dst_unused:UNUSED_PAD src0_sel:WORD_1
	v_cvt_f32_f16_e32 v52, v44
	v_cvt_f32_f16_sdwa v55, v45 dst_sel:DWORD dst_unused:UNUSED_PAD src0_sel:WORD_1
	v_cvt_f32_f16_e32 v54, v45
	v_pk_fma_f32 v[48:49], v[32:33], v[52:53], v[48:49] op_sel_hi:[0,1,1]
	v_pk_fma_f32 v[50:51], v[32:33], v[54:55], v[50:51] op_sel_hi:[0,1,1]
	v_cvt_f32_f16_sdwa v57, v46 dst_sel:DWORD dst_unused:UNUSED_PAD src0_sel:WORD_1
	v_cvt_f32_f16_e32 v56, v46
	v_cvt_f32_f16_sdwa v59, v47 dst_sel:DWORD dst_unused:UNUSED_PAD src0_sel:WORD_1
	v_cvt_f32_f16_e32 v58, v47
	v_pk_fma_f32 v[48:49], v[34:35], v[56:57], v[48:49] op_sel_hi:[0,1,1]
	v_pk_fma_f32 v[50:51], v[34:35], v[58:59], v[50:51] op_sel_hi:[0,1,1]
	s_branch .Ll2g_loop

.LBB3_55:
	s_waitcnt vmcnt(1)
	v_add_f32_e32 v7, v8, v14
	v_add_f32_e32 v7, v13, v7
	v_mul_f32_e32 v14, 0x3e4ccccd, v7
	v_cmp_lt_f32_e32 vcc, 0, v7
	s_nop 1
	v_cndmask_b32_e32 v7, v14, v7, vcc
	s_or_b64 exec, exec, s[6:7]
	v_mov_b32_e32 v14, 0xff800000
	s_and_saveexec_b64 s[6:7], s[4:5]
	s_cbranch_execnz .LBB3_31
	s_branch .LBB3_32
	s_nop 0
	s_nop 0
	s_nop 0
	s_nop 0
	s_nop 0
	s_nop 0
	s_nop 0
	s_nop 0
	s_nop 0
	s_nop 0
	s_nop 0
	s_nop 0
	s_nop 0
	s_nop 0
	s_nop 0
	s_nop 0
	s_nop 0
	s_nop 0
	s_nop 0
	s_nop 0
	s_nop 0
	s_nop 0
	s_nop 0
	s_nop 0
	s_nop 0
	s_nop 0
	s_nop 0
	s_nop 0
	s_nop 0
	s_nop 0
	s_nop 0
	s_nop 0
	s_nop 0
	s_nop 0
	s_nop 0
	s_nop 0
	s_nop 0
	s_nop 0
	s_nop 0
	s_nop 0
	s_nop 0
	s_nop 0
	s_nop 0
	s_nop 0
	s_nop 0
	s_nop 0
	s_nop 0
	s_nop 0
	s_nop 0
	s_nop 0
	s_nop 0
	s_nop 0
	s_nop 0
	s_nop 0
	s_nop 0
	s_nop 0
	s_nop 0
	s_endpgm
